# LayerNorm-2 row sums (phase 10): xor-butterfly wave_sum through 6 ds_bpermute round trips replaced by the same butterfly in registers (DPP quad_perm/row_half_mirror/row_mirror + v_permlane16/32_swap),
# speedup vs baseline: 1.0195x; 1.0037x over previous
.LBB0_1666:
	s_add_i32 s6, s20, -7
	v_readlane_b32 s4, v86, s6
	v_lshl_add_u64 v[56:57], s[8:9], 0, v[54:55]
	s_ashr_i32 s5, s4, 31
	v_add_co_u32_e32 v58, vcc, 0x35b00000, v56
	s_lshl_b64 s[4:5], s[4:5], 10
	s_nop 0
	v_addc_co_u32_e32 v59, vcc, 0, v57, vcc
	s_waitcnt vmcnt(8)
	v_readlane_b32 s6, v37, s6
	v_lshl_add_u64 v[32:33], v[42:43], 0, s[4:5]
	global_load_dwordx2 v[74:75], v[58:59], off nt
	global_load_dwordx2 v[78:79], v[58:59], off offset:512 nt
	global_load_dwordx2 v[72:73], v[58:59], off offset:1024 nt
	global_load_dwordx2 v[62:63], v[58:59], off offset:1536 nt
	v_mul_f32_e32 v34, s6, v229
	global_load_dword v84, v[32:33], off nt
	global_load_dword v106, v[32:33], off offset:256 nt
	global_load_dword v82, v[32:33], off offset:512 nt
	global_load_dword v35, v[32:33], off offset:768 nt
	s_add_i32 s6, s20, -6
	v_readlane_b32 s4, v86, s6
	s_ashr_i32 s5, s4, 31
	v_readlane_b32 s6, v37, s6
	s_lshl_b64 s[4:5], s[4:5], 10
	v_lshl_add_u64 v[60:61], v[42:43], 0, s[4:5]
	v_mul_f32_e32 v32, s6, v229
	s_add_i32 s6, s20, -5
	global_load_dword v107, v[60:61], off nt
	global_load_dword v108, v[60:61], off offset:256 nt
	global_load_dword v71, v[60:61], off offset:512 nt
	global_load_dword v33, v[60:61], off offset:768 nt
	v_readlane_b32 s4, v86, s6
	s_ashr_i32 s5, s4, 31
	s_lshl_b64 s[4:5], s[4:5], 10
	v_lshl_add_u64 v[60:61], v[42:43], 0, s[4:5]
	global_load_dword v109, v[60:61], off nt
	global_load_dword v110, v[60:61], off offset:256 nt
	global_load_dword v83, v[60:61], off offset:512 nt
	global_load_dword v69, v[60:61], off offset:768 nt
	v_readlane_b32 s6, v37, s6
	s_add_i32 s7, s20, -2
	s_add_i32 s21, s20, -1
	v_mul_f32_e32 v68, s6, v229
	s_add_i32 s6, s20, -4
	v_readlane_b32 s4, v86, s6
	s_ashr_i32 s5, s4, 31
	s_lshl_b64 s[4:5], s[4:5], 10
	v_lshl_add_u64 v[60:61], v[42:43], 0, s[4:5]
	global_load_dword v111, v[60:61], off nt
	global_load_dword v112, v[60:61], off offset:256 nt
	global_load_dword v113, v[60:61], off offset:512 nt
	global_load_dword v85, v[60:61], off offset:768 nt
	global_load_dwordx2 v[66:67], v[58:59], off offset:2048 nt
	global_load_dwordx2 v[64:65], v[58:59], off offset:2560 nt
	s_nop 0
	global_load_dwordx2 v[60:61], v[58:59], off offset:3072 nt
	s_nop 0
	global_load_dwordx2 v[58:59], v[58:59], off offset:3584 nt
	v_readlane_b32 s6, v37, s6
	v_readlane_b32 s22, v37, s20
	s_waitcnt vmcnt(19)
	v_cvt_pk_f32_fp8_e32 v[80:81], v84
	v_mul_f32_e32 v70, s6, v229
	s_add_i32 s6, s20, -3
	v_readlane_b32 s4, v86, s6
	s_ashr_i32 s5, s4, 31
	s_lshl_b64 s[4:5], s[4:5], 10
	v_lshl_add_u64 v[76:77], v[42:43], 0, s[4:5]
	v_readlane_b32 s4, v86, s7
	s_ashr_i32 s5, s4, 31
	s_lshl_b64 s[4:5], s[4:5], 10
	global_load_dword v100, v[76:77], off nt
	global_load_dword v95, v[76:77], off offset:256 nt
	global_load_dword v91, v[76:77], off offset:512 nt
	global_load_dword v87, v[76:77], off offset:768 nt
	v_lshl_add_u64 v[76:77], v[42:43], 0, s[4:5]
	v_readlane_b32 s4, v86, s21
	s_ashr_i32 s5, s4, 31
	s_lshl_b64 s[4:5], s[4:5], 10
	global_load_dword v102, v[76:77], off nt
	global_load_dword v96, v[76:77], off offset:256 nt
	global_load_dword v92, v[76:77], off offset:512 nt
	global_load_dword v88, v[76:77], off offset:768 nt
	v_lshl_add_u64 v[76:77], v[42:43], 0, s[4:5]
	v_readlane_b32 s4, v86, s20
	v_cvt_pk_f32_fp8_sdwa v[104:105], v84 src0_sel:WORD_1
	s_ashr_i32 s5, s4, 31
	s_lshl_b64 s[4:5], s[4:5], 10
	global_load_dword v101, v[76:77], off nt
	global_load_dword v98, v[76:77], off offset:256 nt
	global_load_dword v93, v[76:77], off offset:512 nt
	global_load_dword v89, v[76:77], off offset:768 nt
	v_lshl_add_u64 v[76:77], v[42:43], 0, s[4:5]
	global_load_dword v103, v[76:77], off nt
	global_load_dword v99, v[76:77], off offset:256 nt
	global_load_dword v94, v[76:77], off offset:512 nt
	global_load_dword v90, v[76:77], off offset:768 nt
	v_lshlrev_b32_e32 v76, 16, v74
	v_and_b32_e32 v77, 0xffff0000, v74
	v_lshlrev_b32_e32 v74, 16, v75
	v_and_b32_e32 v75, 0xffff0000, v75
	s_waitcnt vmcnt(32)
	v_pk_mul_f32 v[104:105], v[34:35], v[104:105] op_sel_hi:[0,1]
	v_pk_mul_f32 v[80:81], v[34:35], v[80:81] op_sel_hi:[0,1]
	v_pk_fma_f32 v[76:77], v[76:77], s[0:1], v[80:81] op_sel_hi:[1,0,1]
	v_pk_fma_f32 v[74:75], v[74:75], s[0:1], v[104:105] op_sel_hi:[1,0,1]
	s_waitcnt vmcnt(31)
	v_cvt_pk_f32_fp8_e32 v[80:81], v107
	v_cvt_pk_f32_fp8_sdwa v[104:105], v107 src0_sel:WORD_1
	v_cvt_pk_f32_fp8_sdwa v[114:115], v35 src0_sel:WORD_1
	v_readlane_b32 s6, v37, s6
	s_waitcnt vmcnt(28)
	v_pk_fma_f32 v[76:77], v[32:33], v[80:81], v[76:77] op_sel_hi:[0,1,1]
	v_pk_fma_f32 v[74:75], v[32:33], v[104:105], v[74:75] op_sel_hi:[0,1,1]
	s_waitcnt vmcnt(27)
	v_cvt_pk_f32_fp8_e32 v[80:81], v109
	v_cvt_pk_f32_fp8_sdwa v[104:105], v109 src0_sel:WORD_1
	v_pk_mul_f32 v[114:115], v[34:35], v[114:115] op_sel_hi:[0,1]
	v_readlane_b32 s7, v37, s7
	s_waitcnt vmcnt(24)
	v_pk_fma_f32 v[76:77], v[68:69], v[80:81], v[76:77] op_sel_hi:[0,1,1]
	v_pk_fma_f32 v[74:75], v[68:69], v[104:105], v[74:75] op_sel_hi:[0,1,1]
	s_waitcnt vmcnt(23)
	v_cvt_pk_f32_fp8_e32 v[80:81], v111
	v_cvt_pk_f32_fp8_sdwa v[104:105], v111 src0_sel:WORD_1
	v_readlane_b32 s21, v37, s21
	v_pk_fma_f32 v[76:77], v[70:71], v[80:81], v[76:77] op_sel_hi:[0,1,1]
	v_pk_fma_f32 v[74:75], v[70:71], v[104:105], v[74:75] op_sel_hi:[0,1,1]
	v_pk_mov_b32 v[80:81], v[76:77], v[74:75] op_sel:[1,0]
	v_mov_b32_e32 v104, v76
	v_mov_b32_e32 v105, v75
	v_pk_add_f32 v[80:81], v[80:81], v[104:105]
	v_cvt_pk_f32_fp8_e32 v[104:105], v106
	v_cvt_pk_f32_fp8_sdwa v[106:107], v106 src0_sel:WORD_1
	v_add_f32_e32 v80, v80, v81
	v_add_f32_e32 v84, 0, v80
	v_lshlrev_b32_e32 v80, 16, v78
	v_and_b32_e32 v81, 0xffff0000, v78
	v_lshlrev_b32_e32 v78, 16, v79
	v_and_b32_e32 v79, 0xffff0000, v79
	v_pk_mul_f32 v[106:107], v[34:35], v[106:107] op_sel_hi:[0,1]
	v_pk_mul_f32 v[104:105], v[34:35], v[104:105] op_sel_hi:[0,1]
	v_pk_fma_f32 v[80:81], v[80:81], s[0:1], v[104:105] op_sel_hi:[1,0,1]
	v_pk_fma_f32 v[78:79], v[78:79], s[0:1], v[106:107] op_sel_hi:[1,0,1]
	v_cvt_pk_f32_fp8_e32 v[104:105], v108
	v_cvt_pk_f32_fp8_sdwa v[106:107], v108 src0_sel:WORD_1
	v_cvt_pk_f32_fp8_e32 v[108:109], v82
	v_pk_fma_f32 v[80:81], v[32:33], v[104:105], v[80:81] op_sel_hi:[0,1,1]
	v_pk_fma_f32 v[78:79], v[32:33], v[106:107], v[78:79] op_sel_hi:[0,1,1]
	v_cvt_pk_f32_fp8_e32 v[104:105], v110
	v_cvt_pk_f32_fp8_sdwa v[106:107], v110 src0_sel:WORD_1
	v_cvt_pk_f32_fp8_sdwa v[110:111], v82 src0_sel:WORD_1
	v_pk_mul_f32 v[108:109], v[34:35], v[108:109] op_sel_hi:[0,1]
	v_pk_fma_f32 v[80:81], v[68:69], v[104:105], v[80:81] op_sel_hi:[0,1,1]
	v_pk_fma_f32 v[78:79], v[68:69], v[106:107], v[78:79] op_sel_hi:[0,1,1]
	s_waitcnt vmcnt(22)
	v_cvt_pk_f32_fp8_e32 v[104:105], v112
	v_cvt_pk_f32_fp8_sdwa v[106:107], v112 src0_sel:WORD_1
	v_pk_mul_f32 v[110:111], v[34:35], v[110:111] op_sel_hi:[0,1]
	v_pk_fma_f32 v[80:81], v[70:71], v[104:105], v[80:81] op_sel_hi:[0,1,1]
	v_pk_fma_f32 v[78:79], v[70:71], v[106:107], v[78:79] op_sel_hi:[0,1,1]
	v_pk_mov_b32 v[104:105], v[80:81], v[78:79] op_sel:[1,0]
	v_mov_b32_e32 v106, v80
	v_mov_b32_e32 v107, v79
	v_pk_add_f32 v[104:105], v[104:105], v[106:107]
	v_lshlrev_b32_e32 v106, 16, v72
	v_and_b32_e32 v107, 0xffff0000, v72
	v_pk_fma_f32 v[106:107], v[106:107], s[0:1], v[108:109] op_sel_hi:[1,0,1]
	v_cvt_pk_f32_fp8_e32 v[108:109], v71
	v_lshlrev_b32_e32 v72, 16, v73
	v_and_b32_e32 v73, 0xffff0000, v73
	v_pk_fma_f32 v[72:73], v[72:73], s[0:1], v[110:111] op_sel_hi:[1,0,1]
	v_cvt_pk_f32_fp8_sdwa v[110:111], v71 src0_sel:WORD_1
	v_pk_fma_f32 v[106:107], v[32:33], v[108:109], v[106:107] op_sel_hi:[0,1,1]
	v_cvt_pk_f32_fp8_e32 v[108:109], v83
	v_cvt_pk_f32_fp8_sdwa v[82:83], v83 src0_sel:WORD_1
	v_pk_fma_f32 v[72:73], v[32:33], v[110:111], v[72:73] op_sel_hi:[0,1,1]
	v_lshlrev_b32_e32 v110, 16, v62
	v_pk_fma_f32 v[106:107], v[68:69], v[108:109], v[106:107] op_sel_hi:[0,1,1]
	v_pk_fma_f32 v[72:73], v[68:69], v[82:83], v[72:73] op_sel_hi:[0,1,1]
	s_waitcnt vmcnt(21)
	v_cvt_pk_f32_fp8_e32 v[82:83], v113
	v_cvt_pk_f32_fp8_sdwa v[108:109], v113 src0_sel:WORD_1
	v_cvt_pk_f32_fp8_e32 v[112:113], v35
	v_and_b32_e32 v111, 0xffff0000, v62
	v_lshlrev_b32_e32 v62, 16, v63
	v_and_b32_e32 v63, 0xffff0000, v63
	v_pk_mul_f32 v[34:35], v[34:35], v[112:113] op_sel_hi:[0,1]
	v_pk_fma_f32 v[34:35], v[110:111], s[0:1], v[34:35] op_sel_hi:[1,0,1]
	v_cvt_pk_f32_fp8_e32 v[110:111], v33
	v_cvt_pk_f32_fp8_sdwa v[112:113], v33 src0_sel:WORD_1
	v_pk_fma_f32 v[62:63], v[62:63], s[0:1], v[114:115] op_sel_hi:[1,0,1]
	v_pk_add_f32 v[104:105], v[104:105], v[104:105] op_sel:[0,1] op_sel_hi:[1,0]
	v_pk_fma_f32 v[72:73], v[70:71], v[108:109], v[72:73] op_sel_hi:[0,1,1]
	v_pk_fma_f32 v[62:63], v[32:33], v[112:113], v[62:63] op_sel_hi:[0,1,1]
	v_pk_fma_f32 v[32:33], v[32:33], v[110:111], v[34:35] op_sel_hi:[0,1,1]
	v_cvt_pk_f32_fp8_e32 v[34:35], v69
	v_cvt_pk_f32_fp8_sdwa v[110:111], v69 src0_sel:WORD_1
	v_pk_fma_f32 v[82:83], v[70:71], v[82:83], v[106:107] op_sel_hi:[0,1,1]
	v_add_f32_e32 v106, v82, v83
	v_pk_fma_f32 v[32:33], v[68:69], v[34:35], v[32:33] op_sel_hi:[0,1,1]
	v_pk_fma_f32 v[34:35], v[68:69], v[110:111], v[62:63] op_sel_hi:[0,1,1]
	s_waitcnt vmcnt(20)
	v_cvt_pk_f32_fp8_e32 v[62:63], v85
	v_cvt_pk_f32_fp8_sdwa v[68:69], v85 src0_sel:WORD_1
	v_add_f32_e32 v108, v72, v73
	v_pk_fma_f32 v[68:69], v[70:71], v[68:69], v[34:35] op_sel_hi:[0,1,1]
	v_pk_fma_f32 v[70:71], v[70:71], v[62:63], v[32:33] op_sel_hi:[0,1,1]
	v_mov_b32_e32 v85, v70
	v_mov_b32_e32 v105, v71
	v_mov_b32_e32 v107, v68
	v_mov_b32_e32 v109, v69
	v_pk_add_f32 v[32:33], v[84:85], v[104:105]
	v_pk_add_f32 v[34:35], v[106:107], v[108:109]
	s_nop 0
	v_pk_add_f32 v[32:33], v[32:33], v[34:35]
	s_nop 0
	v_add_f32_e32 v32, v32, v33
	s_nop 1
	v_add_f32_dpp v32, v32, v32 quad_perm:[1,0,3,2] row_mask:0xf bank_mask:0xf
	s_nop 1
	v_add_f32_dpp v32, v32, v32 quad_perm:[2,3,0,1] row_mask:0xf bank_mask:0xf
	s_nop 1
	v_add_f32_dpp v32, v32, v32 row_half_mirror row_mask:0xf bank_mask:0xf
	s_nop 1
	v_add_f32_dpp v32, v32, v32 row_mirror row_mask:0xf bank_mask:0xf
	s_nop 1
	v_mov_b32_e32 v33, v32
	s_nop 1
	v_permlane16_swap_b32_e32 v33, v32
	s_nop 1
	v_add_f32_e32 v32, v32, v33
	s_nop 1
	v_mov_b32_e32 v33, v32
	s_nop 1
	v_permlane32_swap_b32_e32 v33, v32
	s_nop 1
	v_add_f32_e32 v104, v32, v33
	v_fmamk_f32 v77, v104, 0xba800000, v77
	v_fmac_f32_e32 v76, 0xba800000, v104
	v_fmamk_f32 v75, v104, 0xba800000, v75
	v_fmac_f32_e32 v74, 0xba800000, v104
	v_pk_mul_f32 v[32:33], v[74:75], v[74:75]
	v_pk_mul_f32 v[34:35], v[76:77], v[76:77]
	v_fmamk_f32 v79, v104, 0xba800000, v79
	v_pk_mov_b32 v[62:63], v[34:35], v[32:33] op_sel:[1,0]
	v_mov_b32_e32 v35, v33
	v_pk_add_f32 v[32:33], v[62:63], v[34:35]
	v_fmac_f32_e32 v78, 0xba800000, v104
	v_fmamk_f32 v81, v104, 0xba800000, v81
	v_fmac_f32_e32 v80, 0xba800000, v104
	v_pk_add_f32 v[32:33], v[32:33], v[32:33] op_sel_hi:[0,1]
	v_pk_mul_f32 v[34:35], v[78:79], v[78:79]
	v_pk_mul_f32 v[62:63], v[80:81], v[80:81]
	v_fmac_f32_e32 v82, 0xba800000, v104
	v_pk_mov_b32 v[84:85], v[62:63], v[34:35] op_sel:[1,0]
	v_mov_b32_e32 v63, v35
	v_fmac_f32_e32 v72, 0xba800000, v104
	v_fmamk_f32 v83, v104, 0xba800000, v83
	v_mul_f32_e32 v32, v82, v82
	v_pk_add_f32 v[34:35], v[84:85], v[62:63]
	v_fmamk_f32 v73, v104, 0xba800000, v73
	v_pk_fma_f32 v[62:63], v[82:83], v[82:83], v[32:33] op_sel_hi:[1,1,0]
	v_mul_f32_e32 v32, v72, v72
	v_pk_add_f32 v[34:35], v[34:35], v[34:35] op_sel_hi:[0,1]
	v_pk_fma_f32 v[84:85], v[72:73], v[72:73], v[32:33] op_sel_hi:[1,1,0]
	v_fmamk_f32 v69, v104, 0xba800000, v69
	v_fmac_f32_e32 v68, 0xba800000, v104
	v_fmamk_f32 v71, v104, 0xba800000, v71
	v_fmac_f32_e32 v70, 0xba800000, v104
	v_mul_f32_e32 v62, v70, v70
	v_mul_f32_e32 v84, v71, v71
	v_mul_f32_e32 v32, v68, v68
	v_mul_f32_e32 v34, v69, v69
	v_pk_add_f32 v[62:63], v[62:63], v[84:85]
	v_pk_add_f32 v[32:33], v[32:33], v[34:35]
	s_nop 0
	v_pk_add_f32 v[32:33], v[62:63], v[32:33]
	s_nop 0
	v_add_f32_e32 v32, v32, v33
	s_nop 1
	v_add_f32_dpp v32, v32, v32 quad_perm:[1,0,3,2] row_mask:0xf bank_mask:0xf
	s_nop 1
	v_add_f32_dpp v32, v32, v32 quad_perm:[2,3,0,1] row_mask:0xf bank_mask:0xf
	s_nop 1
	v_add_f32_dpp v32, v32, v32 row_half_mirror row_mask:0xf bank_mask:0xf
	s_nop 1
	v_add_f32_dpp v32, v32, v32 row_mirror row_mask:0xf bank_mask:0xf
	s_nop 1
	v_mov_b32_e32 v33, v32
	s_nop 1
	v_permlane16_swap_b32_e32 v33, v32
	s_nop 1
	v_add_f32_e32 v32, v32, v33
	s_nop 1
	v_mov_b32_e32 v33, v32
	s_nop 1
	v_permlane32_swap_b32_e32 v33, v32
	s_nop 1
	v_add_f32_e32 v32, v32, v33
	v_fmamk_f32 v32, v32, 0x3a800000, v224
	v_cmp_gt_f32_e32 vcc, s1, v32
	v_mul_f32_e32 v33, 0x4f800000, v32
	s_nop 0
	v_cndmask_b32_e32 v32, v32, v33, vcc
	v_sqrt_f32_e32 v33, v32
	s_nop 0
	v_add_u32_e32 v34, -1, v33
	v_fma_f32 v35, -v34, v33, v32
	v_cmp_ge_f32_e64 s[4:5], 0, v35
	v_add_u32_e32 v35, 1, v33
	s_nop 0
	v_cndmask_b32_e64 v34, v33, v34, s[4:5]
	v_fma_f32 v33, -v35, v33, v32
	v_cmp_lt_f32_e64 s[4:5], 0, v33
	s_nop 1
	v_cndmask_b32_e64 v33, v34, v35, s[4:5]
	v_mul_f32_e32 v34, 0x37800000, v33
	v_cndmask_b32_e32 v33, v33, v34, vcc
	v_cmp_class_f32_e32 vcc, v32, v240
	s_nop 1
	v_cndmask_b32_e32 v32, v33, v32, vcc
	v_div_scale_f32 v33, s[4:5], v32, v32, 1.0
	v_rcp_f32_e32 v34, v33
	s_nop 0
	v_fma_f32 v35, -v33, v34, 1.0
	v_fmac_f32_e32 v34, v35, v34
	v_div_scale_f32 v35, vcc, 1.0, v32, 1.0
	v_mul_f32_e32 v62, v35, v34
	v_fma_f32 v63, -v33, v62, v35
	v_fmac_f32_e32 v62, v63, v34
	v_fma_f32 v33, -v33, v62, v35
	v_div_fmas_f32 v33, v33, v34, v62
	v_div_fixup_f32 v84, v33, v32, 1.0
	v_pk_mul_f32 v[32:33], v[76:77], v[84:85] op_sel_hi:[1,0]
	v_pk_mul_f32 v[34:35], v[74:75], v[84:85] op_sel_hi:[1,0]
	v_pk_fma_f32 v[32:33], v[0:1], v[32:33], v[8:9]
	v_pk_fma_f32 v[34:35], v[2:3], v[34:35], v[10:11]
	v_add_co_u32_e32 v74, vcc, 0x33b00000, v56
	v_cvt_pk_bf16_f32 v62, v32, v33
	v_cvt_pk_bf16_f32 v63, v34, v35
	v_addc_co_u32_e32 v75, vcc, 0, v57, vcc
	global_store_dwordx2 v[74:75], v[62:63], off
	v_mov_b32_e32 v74, 0
	v_cvt_pk_fp8_f32 v74, v32, v33
	v_lshl_add_u64 v[62:63], s[8:9], 0, v[52:53]
	s_andn2_b64 vcc, exec, s[18:19]
	v_cvt_pk_fp8_f32 v74, v34, v35 op_sel:[0,0,1]
	global_store_dword v[62:63], v74, off offset:-1024
	v_cndmask_b32_e64 v74, 0, 1, s[18:19]
	v_cmp_ne_u32_e64 s[4:5], 1, v74
	s_cbranch_vccnz .LBB0_1668
	v_add_co_u32_e32 v74, vcc, 0xfffff000, v50
	s_nop 1
	v_addc_co_u32_e32 v75, vcc, -1, v51, vcc
	global_store_dwordx4 v[74:75], v[32:35], off offset:-3072

.LBB0_1674:
	s_waitcnt vmcnt(27)
	s_nop 0
	v_lshlrev_b32_e32 v32, 16, v66
	v_and_b32_e32 v33, 0xffff0000, v66
	v_lshlrev_b32_e32 v34, 16, v67
	v_and_b32_e32 v35, 0xffff0000, v67
	s_waitcnt vmcnt(23)
	v_cvt_pk_f32_fp8_e32 v[66:67], v100
	v_cvt_pk_f32_fp8_sdwa v[68:69], v100 src0_sel:WORD_1
	v_mul_f32_e32 v76, s6, v229
	v_mul_f32_e32 v74, s7, v229
	v_pk_mul_f32 v[66:67], v[76:77], v[66:67] op_sel_hi:[0,1]
	v_pk_mul_f32 v[68:69], v[76:77], v[68:69] op_sel_hi:[0,1]
	v_pk_fma_f32 v[32:33], v[32:33], s[0:1], v[66:67] op_sel_hi:[1,0,1]
	v_pk_fma_f32 v[34:35], v[34:35], s[0:1], v[68:69] op_sel_hi:[1,0,1]
	s_waitcnt vmcnt(19)
	v_cvt_pk_f32_fp8_e32 v[66:67], v102
	v_cvt_pk_f32_fp8_sdwa v[68:69], v102 src0_sel:WORD_1
	v_mul_f32_e32 v72, s21, v229
	v_mul_f32_e32 v70, s22, v229
	v_pk_fma_f32 v[32:33], v[74:75], v[66:67], v[32:33] op_sel_hi:[0,1,1]
	v_pk_fma_f32 v[34:35], v[74:75], v[68:69], v[34:35] op_sel_hi:[0,1,1]
	s_waitcnt vmcnt(15)
	v_cvt_pk_f32_fp8_e32 v[66:67], v101
	v_cvt_pk_f32_fp8_sdwa v[68:69], v101 src0_sel:WORD_1
	v_cvt_pk_f32_fp8_sdwa v[80:81], v95 src0_sel:WORD_1
	v_cvt_pk_f32_fp8_e32 v[82:83], v91
	v_pk_fma_f32 v[66:67], v[72:73], v[66:67], v[32:33] op_sel_hi:[0,1,1]
	v_pk_fma_f32 v[32:33], v[72:73], v[68:69], v[34:35] op_sel_hi:[0,1,1]
	s_waitcnt vmcnt(11)
	v_cvt_pk_f32_fp8_e32 v[34:35], v103
	v_cvt_pk_f32_fp8_sdwa v[68:69], v103 src0_sel:WORD_1
	v_pk_mul_f32 v[80:81], v[76:77], v[80:81] op_sel_hi:[0,1]
	v_cvt_pk_f32_fp8_sdwa v[84:85], v91 src0_sel:WORD_1
	v_pk_fma_f32 v[34:35], v[70:71], v[34:35], v[66:67] op_sel_hi:[0,1,1]
	v_pk_fma_f32 v[32:33], v[70:71], v[68:69], v[32:33] op_sel_hi:[0,1,1]
	v_pk_mov_b32 v[66:67], v[34:35], v[32:33] op_sel:[1,0]
	v_mov_b32_e32 v68, v34
	v_mov_b32_e32 v69, v33
	v_pk_add_f32 v[66:67], v[66:67], v[68:69]
	v_cvt_pk_f32_fp8_e32 v[68:69], v95
	v_add_f32_e32 v66, v66, v67
	v_add_f32_e32 v78, 0, v66
	v_lshlrev_b32_e32 v66, 16, v64
	v_and_b32_e32 v67, 0xffff0000, v64
	v_lshlrev_b32_e32 v64, 16, v65
	v_and_b32_e32 v65, 0xffff0000, v65
	v_pk_mul_f32 v[68:69], v[76:77], v[68:69] op_sel_hi:[0,1]
	v_pk_fma_f32 v[66:67], v[66:67], s[0:1], v[68:69] op_sel_hi:[1,0,1]
	v_pk_fma_f32 v[64:65], v[64:65], s[0:1], v[80:81] op_sel_hi:[1,0,1]
	v_cvt_pk_f32_fp8_e32 v[68:69], v96
	v_cvt_pk_f32_fp8_sdwa v[80:81], v96 src0_sel:WORD_1
	v_pk_mul_f32 v[84:85], v[76:77], v[84:85] op_sel_hi:[0,1]
	v_pk_mul_f32 v[82:83], v[76:77], v[82:83] op_sel_hi:[0,1]
	v_pk_fma_f32 v[66:67], v[74:75], v[68:69], v[66:67] op_sel_hi:[0,1,1]
	v_pk_fma_f32 v[64:65], v[74:75], v[80:81], v[64:65] op_sel_hi:[0,1,1]
	v_cvt_pk_f32_fp8_e32 v[68:69], v98
	v_cvt_pk_f32_fp8_sdwa v[80:81], v98 src0_sel:WORD_1
	v_pk_fma_f32 v[66:67], v[72:73], v[68:69], v[66:67] op_sel_hi:[0,1,1]
	v_pk_fma_f32 v[64:65], v[72:73], v[80:81], v[64:65] op_sel_hi:[0,1,1]
	s_waitcnt vmcnt(10)
	v_cvt_pk_f32_fp8_e32 v[68:69], v99
	v_cvt_pk_f32_fp8_sdwa v[80:81], v99 src0_sel:WORD_1
	v_cvt_pk_f32_fp8_sdwa v[98:99], v87 src0_sel:WORD_1
	v_pk_fma_f32 v[66:67], v[70:71], v[68:69], v[66:67] op_sel_hi:[0,1,1]
	v_pk_fma_f32 v[64:65], v[70:71], v[80:81], v[64:65] op_sel_hi:[0,1,1]
	v_pk_mov_b32 v[68:69], v[66:67], v[64:65] op_sel:[1,0]
	v_mov_b32_e32 v80, v66
	v_mov_b32_e32 v81, v65
	v_pk_add_f32 v[68:69], v[68:69], v[80:81]
	v_pk_mul_f32 v[98:99], v[76:77], v[98:99] op_sel_hi:[0,1]
	v_pk_add_f32 v[80:81], v[68:69], v[68:69] op_sel:[0,1] op_sel_hi:[1,0]
	v_lshlrev_b32_e32 v68, 16, v60
	v_and_b32_e32 v69, 0xffff0000, v60
	v_lshlrev_b32_e32 v60, 16, v61
	v_and_b32_e32 v61, 0xffff0000, v61
	v_pk_fma_f32 v[68:69], v[68:69], s[0:1], v[82:83] op_sel_hi:[1,0,1]
	v_pk_fma_f32 v[60:61], v[60:61], s[0:1], v[84:85] op_sel_hi:[1,0,1]
	v_cvt_pk_f32_fp8_e32 v[82:83], v92
	v_cvt_pk_f32_fp8_sdwa v[84:85], v92 src0_sel:WORD_1
	v_lshlrev_b32_e32 v92, 16, v58
	v_pk_fma_f32 v[68:69], v[74:75], v[82:83], v[68:69] op_sel_hi:[0,1,1]
	v_pk_fma_f32 v[60:61], v[74:75], v[84:85], v[60:61] op_sel_hi:[0,1,1]
	v_cvt_pk_f32_fp8_e32 v[82:83], v93
	v_cvt_pk_f32_fp8_sdwa v[84:85], v93 src0_sel:WORD_1
	v_and_b32_e32 v93, 0xffff0000, v58
	v_lshlrev_b32_e32 v58, 16, v59
	v_pk_fma_f32 v[68:69], v[72:73], v[82:83], v[68:69] op_sel_hi:[0,1,1]
	v_pk_fma_f32 v[60:61], v[72:73], v[84:85], v[60:61] op_sel_hi:[0,1,1]
	s_waitcnt vmcnt(9)
	v_cvt_pk_f32_fp8_e32 v[82:83], v94
	v_cvt_pk_f32_fp8_sdwa v[84:85], v94 src0_sel:WORD_1
	v_cvt_pk_f32_fp8_e32 v[94:95], v87
	v_and_b32_e32 v59, 0xffff0000, v59
	v_pk_fma_f32 v[58:59], v[58:59], s[0:1], v[98:99] op_sel_hi:[1,0,1]
	v_pk_fma_f32 v[60:61], v[70:71], v[84:85], v[60:61] op_sel_hi:[0,1,1]
	v_pk_mul_f32 v[76:77], v[76:77], v[94:95] op_sel_hi:[0,1]
	v_pk_fma_f32 v[76:77], v[92:93], s[0:1], v[76:77] op_sel_hi:[1,0,1]
	v_cvt_pk_f32_fp8_e32 v[92:93], v88
	v_cvt_pk_f32_fp8_sdwa v[94:95], v88 src0_sel:WORD_1
	v_pk_fma_f32 v[68:69], v[70:71], v[82:83], v[68:69] op_sel_hi:[0,1,1]
	v_add_f32_e32 v82, v68, v69
	v_add_f32_e32 v84, v60, v61
	v_pk_fma_f32 v[58:59], v[74:75], v[94:95], v[58:59] op_sel_hi:[0,1,1]
	v_pk_fma_f32 v[74:75], v[74:75], v[92:93], v[76:77] op_sel_hi:[0,1,1]
	v_cvt_pk_f32_fp8_e32 v[76:77], v89
	v_cvt_pk_f32_fp8_sdwa v[88:89], v89 src0_sel:WORD_1
	v_pk_fma_f32 v[74:75], v[72:73], v[76:77], v[74:75] op_sel_hi:[0,1,1]
	v_pk_fma_f32 v[58:59], v[72:73], v[88:89], v[58:59] op_sel_hi:[0,1,1]
	s_waitcnt vmcnt(8)
	v_cvt_pk_f32_fp8_e32 v[72:73], v90
	v_cvt_pk_f32_fp8_sdwa v[76:77], v90 src0_sel:WORD_1
	v_pk_fma_f32 v[58:59], v[70:71], v[76:77], v[58:59] op_sel_hi:[0,1,1]
	v_pk_fma_f32 v[70:71], v[70:71], v[72:73], v[74:75] op_sel_hi:[0,1,1]
	v_mov_b32_e32 v79, v70
	v_mov_b32_e32 v81, v71
	v_mov_b32_e32 v83, v58
	v_mov_b32_e32 v85, v59
	v_pk_add_f32 v[72:73], v[78:79], v[80:81]
	v_pk_add_f32 v[74:75], v[82:83], v[84:85]
	s_nop 0
	v_pk_add_f32 v[72:73], v[72:73], v[74:75]
	s_nop 0
	v_add_f32_e32 v72, v72, v73
	s_nop 1
	v_add_f32_dpp v72, v72, v72 quad_perm:[1,0,3,2] row_mask:0xf bank_mask:0xf
	s_nop 1
	v_add_f32_dpp v72, v72, v72 quad_perm:[2,3,0,1] row_mask:0xf bank_mask:0xf
	s_nop 1
	v_add_f32_dpp v72, v72, v72 row_half_mirror row_mask:0xf bank_mask:0xf
	s_nop 1
	v_add_f32_dpp v72, v72, v72 row_mirror row_mask:0xf bank_mask:0xf
	s_nop 1
	v_mov_b32_e32 v73, v72
	s_nop 1
	v_permlane16_swap_b32_e32 v73, v72
	s_nop 1
	v_add_f32_e32 v72, v72, v73
	s_nop 1
	v_mov_b32_e32 v73, v72
	s_nop 1
	v_permlane32_swap_b32_e32 v73, v72
	s_nop 1
	v_add_f32_e32 v80, v72, v73
	v_fmamk_f32 v35, v80, 0xba800000, v35
	v_fmac_f32_e32 v34, 0xba800000, v80
	v_fmamk_f32 v33, v80, 0xba800000, v33
	v_fmac_f32_e32 v32, 0xba800000, v80
	v_pk_mul_f32 v[72:73], v[32:33], v[32:33]
	v_pk_mul_f32 v[74:75], v[34:35], v[34:35]
	v_fmamk_f32 v65, v80, 0xba800000, v65
	v_pk_mov_b32 v[76:77], v[74:75], v[72:73] op_sel:[1,0]
	v_mov_b32_e32 v75, v73
	v_pk_add_f32 v[72:73], v[76:77], v[74:75]
	v_fmac_f32_e32 v64, 0xba800000, v80
	v_fmamk_f32 v67, v80, 0xba800000, v67
	v_fmac_f32_e32 v66, 0xba800000, v80
	v_pk_add_f32 v[72:73], v[72:73], v[72:73] op_sel_hi:[0,1]
	v_pk_mul_f32 v[74:75], v[64:65], v[64:65]
	v_pk_mul_f32 v[76:77], v[66:67], v[66:67]
	v_fmac_f32_e32 v68, 0xba800000, v80
	v_pk_mov_b32 v[78:79], v[76:77], v[74:75] op_sel:[1,0]
	v_mov_b32_e32 v77, v75
	v_fmac_f32_e32 v60, 0xba800000, v80
	v_fmamk_f32 v69, v80, 0xba800000, v69
	v_mul_f32_e32 v72, v68, v68
	v_pk_add_f32 v[74:75], v[78:79], v[76:77]
	v_fmamk_f32 v61, v80, 0xba800000, v61
	v_pk_fma_f32 v[76:77], v[68:69], v[68:69], v[72:73] op_sel_hi:[1,1,0]
	v_mul_f32_e32 v72, v60, v60
	v_pk_add_f32 v[74:75], v[74:75], v[74:75] op_sel_hi:[0,1]
	v_pk_fma_f32 v[78:79], v[60:61], v[60:61], v[72:73] op_sel_hi:[1,1,0]
	v_fmamk_f32 v59, v80, 0xba800000, v59
	v_fmac_f32_e32 v58, 0xba800000, v80
	v_fmamk_f32 v71, v80, 0xba800000, v71
	v_fmac_f32_e32 v70, 0xba800000, v80
	v_mul_f32_e32 v76, v70, v70
	v_mul_f32_e32 v78, v71, v71
	v_mul_f32_e32 v72, v58, v58
	v_mul_f32_e32 v74, v59, v59
	v_pk_add_f32 v[76:77], v[76:77], v[78:79]
	v_pk_add_f32 v[72:73], v[72:73], v[74:75]
	s_nop 0
	v_pk_add_f32 v[72:73], v[76:77], v[72:73]
	s_nop 0
	v_add_f32_e32 v72, v72, v73
	s_nop 1
	v_add_f32_dpp v72, v72, v72 quad_perm:[1,0,3,2] row_mask:0xf bank_mask:0xf
	s_nop 1
	v_add_f32_dpp v72, v72, v72 quad_perm:[2,3,0,1] row_mask:0xf bank_mask:0xf
	s_nop 1
	v_add_f32_dpp v72, v72, v72 row_half_mirror row_mask:0xf bank_mask:0xf
	s_nop 1
	v_add_f32_dpp v72, v72, v72 row_mirror row_mask:0xf bank_mask:0xf
	s_nop 1
	v_mov_b32_e32 v73, v72
	s_nop 1
	v_permlane16_swap_b32_e32 v73, v72
	s_nop 1
	v_add_f32_e32 v72, v72, v73
	s_nop 1
	v_mov_b32_e32 v73, v72
	s_nop 1
	v_permlane32_swap_b32_e32 v73, v72
	s_nop 1
	v_add_f32_e32 v72, v72, v73
	v_fmamk_f32 v72, v72, 0x3a800000, v224
	v_cmp_gt_f32_e32 vcc, s1, v72
	v_mul_f32_e32 v73, 0x4f800000, v72
	s_nop 0
	v_cndmask_b32_e32 v72, v72, v73, vcc
	v_sqrt_f32_e32 v73, v72
	s_nop 0
	v_add_u32_e32 v74, -1, v73
	v_fma_f32 v75, -v74, v73, v72
	v_cmp_ge_f32_e64 s[6:7], 0, v75
	v_add_u32_e32 v75, 1, v73
	s_nop 0
	v_cndmask_b32_e64 v74, v73, v74, s[6:7]
	v_fma_f32 v73, -v75, v73, v72
	v_cmp_lt_f32_e64 s[6:7], 0, v73
	s_nop 1
	v_cndmask_b32_e64 v73, v74, v75, s[6:7]
	v_mul_f32_e32 v74, 0x37800000, v73
	v_cndmask_b32_e32 v73, v73, v74, vcc
	v_cmp_class_f32_e32 vcc, v72, v240
	s_nop 1
	v_cndmask_b32_e32 v72, v73, v72, vcc
	v_div_scale_f32 v73, s[6:7], v72, v72, 1.0
	v_rcp_f32_e32 v74, v73
	s_nop 0
	v_fma_f32 v75, -v73, v74, 1.0
	v_fmac_f32_e32 v74, v75, v74
	v_div_scale_f32 v75, vcc, 1.0, v72, 1.0
	v_mul_f32_e32 v76, v75, v74
	v_fma_f32 v77, -v73, v76, v75
	v_fmac_f32_e32 v76, v77, v74
	v_fma_f32 v73, -v73, v76, v75
	v_div_fmas_f32 v73, v73, v74, v76
	v_div_fixup_f32 v72, v73, v72, 1.0
	v_pk_mul_f32 v[74:75], v[34:35], v[72:73] op_sel_hi:[1,0]
	v_pk_mul_f32 v[32:33], v[32:33], v[72:73] op_sel_hi:[1,0]
	v_mov_b32_e32 v73, 0
	v_pk_fma_f32 v[34:35], v[2:3], v[32:33], v[10:11]
	v_pk_fma_f32 v[32:33], v[0:1], v[74:75], v[8:9]
	v_add_co_u32_e32 v76, vcc, 0x33b00000, v56
	v_cvt_pk_fp8_f32 v73, v32, v33
	s_nop 0
	v_addc_co_u32_e32 v77, vcc, 0, v57, vcc
	v_cvt_pk_bf16_f32 v74, v32, v33
	v_cvt_pk_fp8_f32 v73, v34, v35 op_sel:[0,0,1]
	v_cvt_pk_bf16_f32 v75, v34, v35
	s_and_b64 vcc, exec, s[4:5]
	global_store_dwordx2 v[76:77], v[74:75], off offset:2048
	global_store_dword v[62:63], v73, off
	s_cbranch_vccnz .LBB0_1676
	global_store_dwordx4 v[50:51], v[32:35], off offset:-3072
